# v16_clean
# speedup vs baseline: 1.0362x; 1.0082x over previous
.LBB1_65:
	s_or_b64 exec, exec, s[2:3]
	s_waitcnt lgkmcnt(0)
	s_barrier
	ds_read2st64_b32 v[76:77], v223 offset1:2
	v_add_u32_e32 v67, v222, v224
	s_cmp_eq_u64 s[6:7], 0
	s_cbranch_scc0 .Lep1_k1
	v_mov_b32_e32 v18, 0
	v_mov_b32_e32 v19, 0
	v_mov_b32_e32 v20, 0
	v_mov_b32_e32 v21, 0
	ds_read2st64_b32 v[50:51], v221 offset0:0 offset1:1
	ds_read2st64_b32 v[52:53], v221 offset0:2 offset1:3
	ds_read2st64_b32 v[54:55], v221 offset0:4 offset1:5
	ds_read2st64_b32 v[56:57], v221 offset0:6 offset1:7
	ds_read2st64_b32 v[58:59], v221 offset0:8 offset1:9
	ds_read2st64_b32 v[60:61], v221 offset0:10 offset1:11
	ds_read2st64_b32 v[62:63], v67 offset0:0 offset1:2
	ds_read2st64_b32 v[64:65], v67 offset0:4 offset1:6
	ds_read2st64_b32 v[68:69], v67 offset0:16 offset1:18
	ds_read2st64_b32 v[70:71], v67 offset0:20 offset1:22
	ds_read2st64_b32 v[72:73], v67 offset0:32 offset1:34
	ds_read2st64_b32 v[74:75], v67 offset0:36 offset1:38
	s_waitcnt lgkmcnt(12)
	v_fma_f32 v78, -v76, v77, 0
	s_waitcnt lgkmcnt(4)
	v_pk_add_f32 v[34:35], v[34:35], v[50:51]
	v_pk_add_f32 v[36:37], v[36:37], v[52:53]
	v_pk_add_f32 v[34:35], v[34:35], v[78:79] op_sel_hi:[1,0]
	v_pk_add_f32 v[36:37], v[36:37], v[78:79] op_sel_hi:[1,0]
	v_pk_fma_f32 v[34:35], v[62:63], v[76:77], v[34:35] op_sel:[0,1,0] op_sel_hi:[1,1,1]
	v_pk_fma_f32 v[36:37], v[64:65], v[76:77], v[36:37] op_sel:[0,1,0] op_sel_hi:[1,1,1]
	v_pk_add_f32 v[18:19], v[18:19], v[34:35]
	v_pk_fma_f32 v[20:21], v[34:35], v[34:35], v[20:21]
	v_pk_add_f32 v[18:19], v[18:19], v[36:37]
	v_pk_fma_f32 v[20:21], v[36:37], v[36:37], v[20:21]
	s_waitcnt lgkmcnt(2)
	v_pk_add_f32 v[38:39], v[38:39], v[54:55]
	v_pk_add_f32 v[40:41], v[40:41], v[56:57]
	v_pk_add_f32 v[38:39], v[38:39], v[78:79] op_sel_hi:[1,0]
	v_pk_add_f32 v[40:41], v[40:41], v[78:79] op_sel_hi:[1,0]
	v_pk_fma_f32 v[38:39], v[68:69], v[76:77], v[38:39] op_sel:[0,1,0] op_sel_hi:[1,1,1]
	v_pk_fma_f32 v[40:41], v[70:71], v[76:77], v[40:41] op_sel:[0,1,0] op_sel_hi:[1,1,1]
	v_pk_add_f32 v[18:19], v[18:19], v[38:39]
	v_pk_fma_f32 v[20:21], v[38:39], v[38:39], v[20:21]
	v_pk_add_f32 v[18:19], v[18:19], v[40:41]
	v_pk_fma_f32 v[20:21], v[40:41], v[40:41], v[20:21]
	s_waitcnt lgkmcnt(0)
	v_pk_add_f32 v[42:43], v[42:43], v[58:59]
	v_pk_add_f32 v[44:45], v[44:45], v[60:61]
	v_pk_add_f32 v[42:43], v[42:43], v[78:79] op_sel_hi:[1,0]
	v_pk_add_f32 v[44:45], v[44:45], v[78:79] op_sel_hi:[1,0]
	v_pk_fma_f32 v[42:43], v[72:73], v[76:77], v[42:43] op_sel:[0,1,0] op_sel_hi:[1,1,1]
	v_pk_fma_f32 v[44:45], v[74:75], v[76:77], v[44:45] op_sel:[0,1,0] op_sel_hi:[1,1,1]
	v_pk_add_f32 v[18:19], v[18:19], v[42:43]
	v_pk_fma_f32 v[20:21], v[42:43], v[42:43], v[20:21]
	v_pk_add_f32 v[18:19], v[18:19], v[44:45]
	v_pk_fma_f32 v[20:21], v[44:45], v[44:45], v[20:21]
	ds_read2st64_b32 v[50:51], v221 offset0:12 offset1:13
	ds_read2st64_b32 v[52:53], v221 offset0:14 offset1:15
	ds_read2st64_b32 v[54:55], v221 offset0:16 offset1:17
	ds_read2st64_b32 v[56:57], v221 offset0:18 offset1:19
	ds_read2st64_b32 v[58:59], v221 offset0:20 offset1:21
	ds_read2st64_b32 v[60:61], v221 offset0:22 offset1:23
	ds_read2st64_b32 v[62:63], v67 offset0:48 offset1:50
	ds_read2st64_b32 v[64:65], v67 offset0:52 offset1:54
	ds_read2st64_b32 v[68:69], v67 offset0:64 offset1:66
	ds_read2st64_b32 v[70:71], v67 offset0:68 offset1:70
	ds_read2st64_b32 v[72:73], v67 offset0:80 offset1:82
	ds_read2st64_b32 v[74:75], v67 offset0:84 offset1:86
	s_waitcnt lgkmcnt(4)
	v_pk_add_f32 v[46:47], v[46:47], v[50:51]
	v_pk_add_f32 v[48:49], v[48:49], v[52:53]
	v_pk_add_f32 v[46:47], v[46:47], v[78:79] op_sel_hi:[1,0]
	v_pk_add_f32 v[48:49], v[48:49], v[78:79] op_sel_hi:[1,0]
	v_pk_fma_f32 v[46:47], v[62:63], v[76:77], v[46:47] op_sel:[0,1,0] op_sel_hi:[1,1,1]
	v_pk_fma_f32 v[48:49], v[64:65], v[76:77], v[48:49] op_sel:[0,1,0] op_sel_hi:[1,1,1]
	v_pk_add_f32 v[18:19], v[18:19], v[46:47]
	v_pk_fma_f32 v[20:21], v[46:47], v[46:47], v[20:21]
	v_pk_add_f32 v[18:19], v[18:19], v[48:49]
	v_pk_fma_f32 v[20:21], v[48:49], v[48:49], v[20:21]
	s_waitcnt lgkmcnt(2)
	v_pk_add_f32 v[2:3], v[2:3], v[54:55]
	v_pk_add_f32 v[4:5], v[4:5], v[56:57]
	v_pk_add_f32 v[2:3], v[2:3], v[78:79] op_sel_hi:[1,0]
	v_pk_add_f32 v[4:5], v[4:5], v[78:79] op_sel_hi:[1,0]
	v_pk_fma_f32 v[2:3], v[68:69], v[76:77], v[2:3] op_sel:[0,1,0] op_sel_hi:[1,1,1]
	v_pk_fma_f32 v[4:5], v[70:71], v[76:77], v[4:5] op_sel:[0,1,0] op_sel_hi:[1,1,1]
	v_pk_add_f32 v[18:19], v[18:19], v[2:3]
	v_pk_fma_f32 v[20:21], v[2:3], v[2:3], v[20:21]
	v_pk_add_f32 v[18:19], v[18:19], v[4:5]
	v_pk_fma_f32 v[20:21], v[4:5], v[4:5], v[20:21]
	s_waitcnt lgkmcnt(0)
	v_pk_add_f32 v[6:7], v[6:7], v[58:59]
	v_pk_add_f32 v[8:9], v[8:9], v[60:61]
	v_pk_add_f32 v[6:7], v[6:7], v[78:79] op_sel_hi:[1,0]
	v_pk_add_f32 v[8:9], v[8:9], v[78:79] op_sel_hi:[1,0]
	v_pk_fma_f32 v[6:7], v[72:73], v[76:77], v[6:7] op_sel:[0,1,0] op_sel_hi:[1,1,1]
	v_pk_fma_f32 v[8:9], v[74:75], v[76:77], v[8:9] op_sel:[0,1,0] op_sel_hi:[1,1,1]
	v_pk_add_f32 v[18:19], v[18:19], v[6:7]
	v_pk_fma_f32 v[20:21], v[6:7], v[6:7], v[20:21]
	v_pk_add_f32 v[18:19], v[18:19], v[8:9]
	v_pk_fma_f32 v[20:21], v[8:9], v[8:9], v[20:21]
	v_add_f32_e32 v18, v18, v19
	v_add_f32_e32 v20, v20, v21
	v_mov_b32_e32 v19, v18
	v_mov_b32_e32 v21, v20
	s_nop 1
	v_permlane32_swap_b32_e32 v18, v19
	v_permlane32_swap_b32_e32 v20, v21
	v_add_f32_e32 v18, v18, v19
	v_add_f32_e32 v20, v20, v21
	v_cndmask_b32_e64 v22, v20, v18, s[0:1]
	s_branch .Lep1_join
.Lep1_k1:
	v_mov_b32_e32 v34, 0
	v_mov_b32_e32 v35, 0
	v_mov_b32_e32 v36, 0
	v_mov_b32_e32 v37, 0
	ds_read2st64_b32 v[50:51], v221 offset0:24 offset1:25
	ds_read2st64_b32 v[52:53], v221 offset0:26 offset1:27
	ds_read2st64_b32 v[54:55], v221 offset0:28 offset1:29
	ds_read2st64_b32 v[56:57], v221 offset0:30 offset1:31
	ds_read2st64_b32 v[58:59], v221 offset0:32 offset1:33
	ds_read2st64_b32 v[60:61], v221 offset0:34 offset1:35
	ds_read2st64_b32 v[62:63], v67 offset0:96 offset1:98
	ds_read2st64_b32 v[64:65], v67 offset0:100 offset1:102
	ds_read2st64_b32 v[68:69], v67 offset0:112 offset1:114
	ds_read2st64_b32 v[70:71], v67 offset0:116 offset1:118
	ds_read2st64_b32 v[72:73], v67 offset0:128 offset1:130
	ds_read2st64_b32 v[74:75], v67 offset0:132 offset1:134
	s_waitcnt lgkmcnt(12)
	v_fma_f32 v78, -v76, v77, 0
	s_waitcnt lgkmcnt(4)
	v_pk_add_f32 v[10:11], v[10:11], v[50:51]
	v_pk_add_f32 v[12:13], v[12:13], v[52:53]
	v_pk_add_f32 v[10:11], v[10:11], v[78:79] op_sel_hi:[1,0]
	v_pk_add_f32 v[12:13], v[12:13], v[78:79] op_sel_hi:[1,0]
	v_pk_fma_f32 v[10:11], v[62:63], v[76:77], v[10:11] op_sel:[0,1,0] op_sel_hi:[1,1,1]
	v_pk_fma_f32 v[12:13], v[64:65], v[76:77], v[12:13] op_sel:[0,1,0] op_sel_hi:[1,1,1]
	v_pk_add_f32 v[34:35], v[34:35], v[10:11]
	v_pk_fma_f32 v[36:37], v[10:11], v[10:11], v[36:37]
	v_pk_add_f32 v[34:35], v[34:35], v[12:13]
	v_pk_fma_f32 v[36:37], v[12:13], v[12:13], v[36:37]
	s_waitcnt lgkmcnt(2)
	v_pk_add_f32 v[14:15], v[14:15], v[54:55]
	v_pk_add_f32 v[16:17], v[16:17], v[56:57]
	v_pk_add_f32 v[14:15], v[14:15], v[78:79] op_sel_hi:[1,0]
	v_pk_add_f32 v[16:17], v[16:17], v[78:79] op_sel_hi:[1,0]
	v_pk_fma_f32 v[14:15], v[68:69], v[76:77], v[14:15] op_sel:[0,1,0] op_sel_hi:[1,1,1]
	v_pk_fma_f32 v[16:17], v[70:71], v[76:77], v[16:17] op_sel:[0,1,0] op_sel_hi:[1,1,1]
	v_pk_add_f32 v[34:35], v[34:35], v[14:15]
	v_pk_fma_f32 v[36:37], v[14:15], v[14:15], v[36:37]
	v_pk_add_f32 v[34:35], v[34:35], v[16:17]
	v_pk_fma_f32 v[36:37], v[16:17], v[16:17], v[36:37]
	s_waitcnt lgkmcnt(0)
	v_pk_add_f32 v[18:19], v[18:19], v[58:59]
	v_pk_add_f32 v[20:21], v[20:21], v[60:61]
	v_pk_add_f32 v[18:19], v[18:19], v[78:79] op_sel_hi:[1,0]
	v_pk_add_f32 v[20:21], v[20:21], v[78:79] op_sel_hi:[1,0]
	v_pk_fma_f32 v[18:19], v[72:73], v[76:77], v[18:19] op_sel:[0,1,0] op_sel_hi:[1,1,1]
	v_pk_fma_f32 v[20:21], v[74:75], v[76:77], v[20:21] op_sel:[0,1,0] op_sel_hi:[1,1,1]
	v_pk_add_f32 v[34:35], v[34:35], v[18:19]
	v_pk_fma_f32 v[36:37], v[18:19], v[18:19], v[36:37]
	v_pk_add_f32 v[34:35], v[34:35], v[20:21]
	v_pk_fma_f32 v[36:37], v[20:21], v[20:21], v[36:37]
	ds_read2st64_b32 v[50:51], v221 offset0:36 offset1:37
	ds_read2st64_b32 v[52:53], v221 offset0:38 offset1:39
	ds_read2st64_b32 v[62:63], v67 offset0:144 offset1:146
	ds_read2st64_b32 v[64:65], v67 offset0:148 offset1:150
	s_waitcnt lgkmcnt(0)
	v_pk_add_f32 v[22:23], v[22:23], v[50:51]
	v_pk_add_f32 v[24:25], v[24:25], v[52:53]
	v_pk_add_f32 v[22:23], v[22:23], v[78:79] op_sel_hi:[1,0]
	v_pk_add_f32 v[24:25], v[24:25], v[78:79] op_sel_hi:[1,0]
	v_pk_fma_f32 v[22:23], v[62:63], v[76:77], v[22:23] op_sel:[0,1,0] op_sel_hi:[1,1,1]
	v_pk_fma_f32 v[24:25], v[64:65], v[76:77], v[24:25] op_sel:[0,1,0] op_sel_hi:[1,1,1]
	v_pk_add_f32 v[34:35], v[34:35], v[22:23]
	v_pk_fma_f32 v[36:37], v[22:23], v[22:23], v[36:37]
	v_pk_add_f32 v[34:35], v[34:35], v[24:25]
	v_pk_fma_f32 v[36:37], v[24:25], v[24:25], v[36:37]
	s_mov_b64 s[40:41], exec
	s_and_b64 exec, exec, s[0:1]
	ds_read2st64_b32 v[50:51], v221 offset0:40 offset1:41
	ds_read2st64_b32 v[52:53], v221 offset0:42 offset1:43
	ds_read2st64_b32 v[62:63], v67 offset0:160 offset1:162
	ds_read2st64_b32 v[64:65], v67 offset0:164 offset1:166
	s_waitcnt lgkmcnt(0)
	v_pk_add_f32 v[26:27], v[26:27], v[50:51]
	v_pk_add_f32 v[28:29], v[28:29], v[52:53]
	v_pk_add_f32 v[26:27], v[26:27], v[78:79] op_sel_hi:[1,0]
	v_pk_add_f32 v[28:29], v[28:29], v[78:79] op_sel_hi:[1,0]
	v_pk_fma_f32 v[26:27], v[62:63], v[76:77], v[26:27] op_sel:[0,1,0] op_sel_hi:[1,1,1]
	v_pk_fma_f32 v[28:29], v[64:65], v[76:77], v[28:29] op_sel:[0,1,0] op_sel_hi:[1,1,1]
	v_pk_add_f32 v[34:35], v[34:35], v[26:27]
	v_pk_fma_f32 v[36:37], v[26:27], v[26:27], v[36:37]
	v_pk_add_f32 v[34:35], v[34:35], v[28:29]
	v_pk_fma_f32 v[36:37], v[28:29], v[28:29], v[36:37]
	s_mov_b64 exec, s[40:41]
	v_add_f32_e32 v34, v34, v35
	v_add_f32_e32 v36, v36, v37
	v_mov_b32_e32 v35, v34
	v_mov_b32_e32 v37, v36
	s_nop 1
	v_permlane32_swap_b32_e32 v34, v35
	v_permlane32_swap_b32_e32 v36, v37
	v_add_f32_e32 v34, v34, v35
	v_add_f32_e32 v36, v36, v37
	v_cndmask_b32_e64 v38, v36, v34, s[0:1]
	ds_write_b32 v236, v38

.LBB1_126:
	s_or_b64 exec, exec, s[30:31]
	v_mov_b32_e32 v132, v0
	s_waitcnt lgkmcnt(0)
	s_barrier
	s_lshl_b64 s[2:3], s[36:37], 16
	v_and_b32_e32 v134, 31, v132
	v_lshlrev_b32_e32 v58, 4, v134
	v_add_u32_e32 v59, 0x25680, v58
	v_add_u32_e32 v58, 0x25880, v58
	ds_read_b128 v[62:65], v59
	ds_read_b128 v[58:61], v58
	v_ashrrev_i32_e32 v133, 5, v132
	v_lshlrev_b32_e32 v132, 3, v134
	v_mad_u32_u24 v134, v133, s64, v132
	s_waitcnt lgkmcnt(0)
	v_pk_add_f32 v[54:55], v[54:55], v[62:63] neg_lo:[0,1] neg_hi:[0,1]
	v_pk_add_f32 v[56:57], v[56:57], v[64:65] neg_lo:[0,1] neg_hi:[0,1]
	v_pk_mul_f32 v[54:55], v[58:59], v[54:55]
	v_pk_mul_f32 v[56:57], v[60:61], v[56:57]
	v_pk_add_f32 v[50:51], v[50:51], v[62:63] neg_lo:[0,1] neg_hi:[0,1]
	v_pk_add_f32 v[52:53], v[52:53], v[64:65] neg_lo:[0,1] neg_hi:[0,1]
	v_pk_mul_f32 v[50:51], v[58:59], v[50:51]
	v_pk_mul_f32 v[52:53], v[60:61], v[52:53]
	v_pk_add_f32 v[46:47], v[46:47], v[62:63] neg_lo:[0,1] neg_hi:[0,1]
	v_pk_add_f32 v[48:49], v[48:49], v[64:65] neg_lo:[0,1] neg_hi:[0,1]
	v_pk_mul_f32 v[46:47], v[58:59], v[46:47]
	v_pk_mul_f32 v[48:49], v[60:61], v[48:49]
	v_pk_add_f32 v[42:43], v[42:43], v[62:63] neg_lo:[0,1] neg_hi:[0,1]
	v_pk_add_f32 v[44:45], v[44:45], v[64:65] neg_lo:[0,1] neg_hi:[0,1]
	v_pk_mul_f32 v[42:43], v[58:59], v[42:43]
	v_pk_mul_f32 v[44:45], v[60:61], v[44:45]
	v_pk_add_f32 v[38:39], v[38:39], v[62:63] neg_lo:[0,1] neg_hi:[0,1]
	v_pk_add_f32 v[40:41], v[40:41], v[64:65] neg_lo:[0,1] neg_hi:[0,1]
	v_pk_mul_f32 v[38:39], v[58:59], v[38:39]
	v_pk_mul_f32 v[40:41], v[60:61], v[40:41]
	v_cvt_pk_f16_f32 v54, v54, v55
	v_cvt_pk_f16_f32 v55, v56, v57
	ds_write_b64 v134, v[54:55] offset:43008
	v_cvt_pk_f16_f32 v50, v50, v51
	v_cvt_pk_f16_f32 v51, v52, v53
	ds_write_b64 v134, v[50:51] offset:47360
	v_cvt_pk_f16_f32 v46, v46, v47
	v_cvt_pk_f16_f32 v47, v48, v49
	ds_write_b64 v134, v[46:47] offset:51712
	v_cvt_pk_f16_f32 v42, v42, v43
	v_cvt_pk_f16_f32 v43, v44, v45
	ds_write_b64 v134, v[42:43] offset:56064
	v_cvt_pk_f16_f32 v38, v38, v39
	v_cvt_pk_f16_f32 v39, v40, v41
	ds_write_b64 v134, v[38:39] offset:60416
	v_cmp_gt_i32_e32 vcc, 4, v133
	s_and_saveexec_b64 s[30:31], vcc
	v_pk_add_f32 v[34:35], v[34:35], v[62:63] neg_lo:[0,1] neg_hi:[0,1]
	v_pk_add_f32 v[36:37], v[36:37], v[64:65] neg_lo:[0,1] neg_hi:[0,1]
	v_pk_mul_f32 v[34:35], v[58:59], v[34:35]
	v_pk_mul_f32 v[36:37], v[60:61], v[36:37]
	v_cvt_pk_f16_f32 v34, v34, v35
	v_cvt_pk_f16_f32 v35, v36, v37
	ds_write_b64 v134, v[34:35] offset:64768
	s_or_b64 exec, exec, s[30:31]
	s_waitcnt lgkmcnt(0)
	s_barrier
	v_or_b32_e32 v34, s26, v220
	v_mov_b32_e32 v35, v66
	v_lshl_add_u64 v[34:35], v[34:35], 2, s[28:29]
	v_lshl_add_u64 v[174:175], s[2:3], 1, v[214:215]
	global_load_dword v173, v[34:35], off
	global_load_dwordx4 v[136:139], v[174:175], off
	global_load_dwordx4 v[132:135], v[174:175], off offset:1024
	v_add_u32_e32 v34, v204, v238
	ds_read_b128 v[168:171], v34 offset:43008
	ds_read_b128 v[164:167], v34 offset:43040
	ds_read_b128 v[160:163], v34 offset:43072
	ds_read_b128 v[156:159], v34 offset:43104
	ds_read_b128 v[152:155], v34 offset:43136
	ds_read_b128 v[148:151], v34 offset:43168
	ds_read_b128 v[144:147], v34 offset:43200
	ds_read_b128 v[140:143], v34 offset:43232
	s_mov_b32 s30, 0
	s_mov_b64 s[2:3], -1

.LBB1_146:
	s_or_b64 exec, exec, s[2:3]
	s_waitcnt lgkmcnt(0)
	s_barrier
	ds_read2st64_b32 v[76:77], v223 offset1:2
	v_add_u32_e32 v67, v222, v224
	s_cmp_eq_u64 s[6:7], 0
	s_cbranch_scc0 .Lep2_k1
	v_mov_b32_e32 v18, 0
	v_mov_b32_e32 v19, 0
	v_mov_b32_e32 v20, 0
	v_mov_b32_e32 v21, 0
	ds_read2st64_b32 v[50:51], v221 offset0:0 offset1:1
	ds_read2st64_b32 v[52:53], v221 offset0:2 offset1:3
	ds_read2st64_b32 v[54:55], v221 offset0:4 offset1:5
	ds_read2st64_b32 v[56:57], v221 offset0:6 offset1:7
	ds_read2st64_b32 v[58:59], v221 offset0:8 offset1:9
	ds_read2st64_b32 v[60:61], v221 offset0:10 offset1:11
	ds_read2st64_b32 v[62:63], v67 offset0:0 offset1:2
	ds_read2st64_b32 v[64:65], v67 offset0:4 offset1:6
	ds_read2st64_b32 v[68:69], v67 offset0:16 offset1:18
	ds_read2st64_b32 v[70:71], v67 offset0:20 offset1:22
	ds_read2st64_b32 v[72:73], v67 offset0:32 offset1:34
	ds_read2st64_b32 v[74:75], v67 offset0:36 offset1:38
	s_waitcnt lgkmcnt(12)
	v_fma_f32 v78, -v76, v77, v173
	s_waitcnt lgkmcnt(4)
	v_pk_add_f32 v[34:35], v[34:35], v[50:51]
	v_pk_add_f32 v[36:37], v[36:37], v[52:53]
	v_pk_add_f32 v[34:35], v[34:35], v[78:79] op_sel_hi:[1,0]
	v_pk_add_f32 v[36:37], v[36:37], v[78:79] op_sel_hi:[1,0]
	v_pk_fma_f32 v[34:35], v[62:63], v[76:77], v[34:35] op_sel:[0,1,0] op_sel_hi:[1,1,1]
	v_pk_fma_f32 v[36:37], v[64:65], v[76:77], v[36:37] op_sel:[0,1,0] op_sel_hi:[1,1,1]
	v_pk_add_f32 v[18:19], v[18:19], v[34:35]
	v_pk_fma_f32 v[20:21], v[34:35], v[34:35], v[20:21]
	v_pk_add_f32 v[18:19], v[18:19], v[36:37]
	v_pk_fma_f32 v[20:21], v[36:37], v[36:37], v[20:21]
	s_waitcnt lgkmcnt(2)
	v_pk_add_f32 v[38:39], v[38:39], v[54:55]
	v_pk_add_f32 v[40:41], v[40:41], v[56:57]
	v_pk_add_f32 v[38:39], v[38:39], v[78:79] op_sel_hi:[1,0]
	v_pk_add_f32 v[40:41], v[40:41], v[78:79] op_sel_hi:[1,0]
	v_pk_fma_f32 v[38:39], v[68:69], v[76:77], v[38:39] op_sel:[0,1,0] op_sel_hi:[1,1,1]
	v_pk_fma_f32 v[40:41], v[70:71], v[76:77], v[40:41] op_sel:[0,1,0] op_sel_hi:[1,1,1]
	v_pk_add_f32 v[18:19], v[18:19], v[38:39]
	v_pk_fma_f32 v[20:21], v[38:39], v[38:39], v[20:21]
	v_pk_add_f32 v[18:19], v[18:19], v[40:41]
	v_pk_fma_f32 v[20:21], v[40:41], v[40:41], v[20:21]
	s_waitcnt lgkmcnt(0)
	v_pk_add_f32 v[42:43], v[42:43], v[58:59]
	v_pk_add_f32 v[44:45], v[44:45], v[60:61]
	v_pk_add_f32 v[42:43], v[42:43], v[78:79] op_sel_hi:[1,0]
	v_pk_add_f32 v[44:45], v[44:45], v[78:79] op_sel_hi:[1,0]
	v_pk_fma_f32 v[42:43], v[72:73], v[76:77], v[42:43] op_sel:[0,1,0] op_sel_hi:[1,1,1]
	v_pk_fma_f32 v[44:45], v[74:75], v[76:77], v[44:45] op_sel:[0,1,0] op_sel_hi:[1,1,1]
	v_pk_add_f32 v[18:19], v[18:19], v[42:43]
	v_pk_fma_f32 v[20:21], v[42:43], v[42:43], v[20:21]
	v_pk_add_f32 v[18:19], v[18:19], v[44:45]
	v_pk_fma_f32 v[20:21], v[44:45], v[44:45], v[20:21]
	ds_read2st64_b32 v[50:51], v221 offset0:12 offset1:13
	ds_read2st64_b32 v[52:53], v221 offset0:14 offset1:15
	ds_read2st64_b32 v[54:55], v221 offset0:16 offset1:17
	ds_read2st64_b32 v[56:57], v221 offset0:18 offset1:19
	ds_read2st64_b32 v[58:59], v221 offset0:20 offset1:21
	ds_read2st64_b32 v[60:61], v221 offset0:22 offset1:23
	ds_read2st64_b32 v[62:63], v67 offset0:48 offset1:50
	ds_read2st64_b32 v[64:65], v67 offset0:52 offset1:54
	ds_read2st64_b32 v[68:69], v67 offset0:64 offset1:66
	ds_read2st64_b32 v[70:71], v67 offset0:68 offset1:70
	ds_read2st64_b32 v[72:73], v67 offset0:80 offset1:82
	ds_read2st64_b32 v[74:75], v67 offset0:84 offset1:86
	s_waitcnt lgkmcnt(4)
	v_pk_add_f32 v[46:47], v[46:47], v[50:51]
	v_pk_add_f32 v[48:49], v[48:49], v[52:53]
	v_pk_add_f32 v[46:47], v[46:47], v[78:79] op_sel_hi:[1,0]
	v_pk_add_f32 v[48:49], v[48:49], v[78:79] op_sel_hi:[1,0]
	v_pk_fma_f32 v[46:47], v[62:63], v[76:77], v[46:47] op_sel:[0,1,0] op_sel_hi:[1,1,1]
	v_pk_fma_f32 v[48:49], v[64:65], v[76:77], v[48:49] op_sel:[0,1,0] op_sel_hi:[1,1,1]
	v_pk_add_f32 v[18:19], v[18:19], v[46:47]
	v_pk_fma_f32 v[20:21], v[46:47], v[46:47], v[20:21]
	v_pk_add_f32 v[18:19], v[18:19], v[48:49]
	v_pk_fma_f32 v[20:21], v[48:49], v[48:49], v[20:21]
	s_waitcnt lgkmcnt(2)
	v_pk_add_f32 v[2:3], v[2:3], v[54:55]
	v_pk_add_f32 v[4:5], v[4:5], v[56:57]
	v_pk_add_f32 v[2:3], v[2:3], v[78:79] op_sel_hi:[1,0]
	v_pk_add_f32 v[4:5], v[4:5], v[78:79] op_sel_hi:[1,0]
	v_pk_fma_f32 v[2:3], v[68:69], v[76:77], v[2:3] op_sel:[0,1,0] op_sel_hi:[1,1,1]
	v_pk_fma_f32 v[4:5], v[70:71], v[76:77], v[4:5] op_sel:[0,1,0] op_sel_hi:[1,1,1]
	v_pk_add_f32 v[18:19], v[18:19], v[2:3]
	v_pk_fma_f32 v[20:21], v[2:3], v[2:3], v[20:21]
	v_pk_add_f32 v[18:19], v[18:19], v[4:5]
	v_pk_fma_f32 v[20:21], v[4:5], v[4:5], v[20:21]
	s_waitcnt lgkmcnt(0)
	v_pk_add_f32 v[6:7], v[6:7], v[58:59]
	v_pk_add_f32 v[8:9], v[8:9], v[60:61]
	v_pk_add_f32 v[6:7], v[6:7], v[78:79] op_sel_hi:[1,0]
	v_pk_add_f32 v[8:9], v[8:9], v[78:79] op_sel_hi:[1,0]
	v_pk_fma_f32 v[6:7], v[72:73], v[76:77], v[6:7] op_sel:[0,1,0] op_sel_hi:[1,1,1]
	v_pk_fma_f32 v[8:9], v[74:75], v[76:77], v[8:9] op_sel:[0,1,0] op_sel_hi:[1,1,1]
	v_pk_add_f32 v[18:19], v[18:19], v[6:7]
	v_pk_fma_f32 v[20:21], v[6:7], v[6:7], v[20:21]
	v_pk_add_f32 v[18:19], v[18:19], v[8:9]
	v_pk_fma_f32 v[20:21], v[8:9], v[8:9], v[20:21]
	v_add_f32_e32 v18, v18, v19
	v_add_f32_e32 v20, v20, v21
	v_mov_b32_e32 v19, v18
	v_mov_b32_e32 v21, v20
	s_nop 1
	v_permlane32_swap_b32_e32 v18, v19
	v_permlane32_swap_b32_e32 v20, v21
	v_add_f32_e32 v18, v18, v19
	v_add_f32_e32 v20, v20, v21
	v_cndmask_b32_e64 v22, v20, v18, s[0:1]
	s_branch .Lep2_join
.Lep2_k1:
	v_mov_b32_e32 v34, 0
	v_mov_b32_e32 v35, 0
	v_mov_b32_e32 v36, 0
	v_mov_b32_e32 v37, 0
	ds_read2st64_b32 v[50:51], v221 offset0:24 offset1:25
	ds_read2st64_b32 v[52:53], v221 offset0:26 offset1:27
	ds_read2st64_b32 v[54:55], v221 offset0:28 offset1:29
	ds_read2st64_b32 v[56:57], v221 offset0:30 offset1:31
	ds_read2st64_b32 v[58:59], v221 offset0:32 offset1:33
	ds_read2st64_b32 v[60:61], v221 offset0:34 offset1:35
	ds_read2st64_b32 v[62:63], v67 offset0:96 offset1:98
	ds_read2st64_b32 v[64:65], v67 offset0:100 offset1:102
	ds_read2st64_b32 v[68:69], v67 offset0:112 offset1:114
	ds_read2st64_b32 v[70:71], v67 offset0:116 offset1:118
	ds_read2st64_b32 v[72:73], v67 offset0:128 offset1:130
	ds_read2st64_b32 v[74:75], v67 offset0:132 offset1:134
	s_waitcnt lgkmcnt(12)
	v_fma_f32 v78, -v76, v77, v173
	s_waitcnt lgkmcnt(4)
	v_pk_add_f32 v[10:11], v[10:11], v[50:51]
	v_pk_add_f32 v[12:13], v[12:13], v[52:53]
	v_pk_add_f32 v[10:11], v[10:11], v[78:79] op_sel_hi:[1,0]
	v_pk_add_f32 v[12:13], v[12:13], v[78:79] op_sel_hi:[1,0]
	v_pk_fma_f32 v[10:11], v[62:63], v[76:77], v[10:11] op_sel:[0,1,0] op_sel_hi:[1,1,1]
	v_pk_fma_f32 v[12:13], v[64:65], v[76:77], v[12:13] op_sel:[0,1,0] op_sel_hi:[1,1,1]
	v_pk_add_f32 v[34:35], v[34:35], v[10:11]
	v_pk_fma_f32 v[36:37], v[10:11], v[10:11], v[36:37]
	v_pk_add_f32 v[34:35], v[34:35], v[12:13]
	v_pk_fma_f32 v[36:37], v[12:13], v[12:13], v[36:37]
	s_waitcnt lgkmcnt(2)
	v_pk_add_f32 v[14:15], v[14:15], v[54:55]
	v_pk_add_f32 v[16:17], v[16:17], v[56:57]
	v_pk_add_f32 v[14:15], v[14:15], v[78:79] op_sel_hi:[1,0]
	v_pk_add_f32 v[16:17], v[16:17], v[78:79] op_sel_hi:[1,0]
	v_pk_fma_f32 v[14:15], v[68:69], v[76:77], v[14:15] op_sel:[0,1,0] op_sel_hi:[1,1,1]
	v_pk_fma_f32 v[16:17], v[70:71], v[76:77], v[16:17] op_sel:[0,1,0] op_sel_hi:[1,1,1]
	v_pk_add_f32 v[34:35], v[34:35], v[14:15]
	v_pk_fma_f32 v[36:37], v[14:15], v[14:15], v[36:37]
	v_pk_add_f32 v[34:35], v[34:35], v[16:17]
	v_pk_fma_f32 v[36:37], v[16:17], v[16:17], v[36:37]
	s_waitcnt lgkmcnt(0)
	v_pk_add_f32 v[18:19], v[18:19], v[58:59]
	v_pk_add_f32 v[20:21], v[20:21], v[60:61]
	v_pk_add_f32 v[18:19], v[18:19], v[78:79] op_sel_hi:[1,0]
	v_pk_add_f32 v[20:21], v[20:21], v[78:79] op_sel_hi:[1,0]
	v_pk_fma_f32 v[18:19], v[72:73], v[76:77], v[18:19] op_sel:[0,1,0] op_sel_hi:[1,1,1]
	v_pk_fma_f32 v[20:21], v[74:75], v[76:77], v[20:21] op_sel:[0,1,0] op_sel_hi:[1,1,1]
	v_pk_add_f32 v[34:35], v[34:35], v[18:19]
	v_pk_fma_f32 v[36:37], v[18:19], v[18:19], v[36:37]
	v_pk_add_f32 v[34:35], v[34:35], v[20:21]
	v_pk_fma_f32 v[36:37], v[20:21], v[20:21], v[36:37]
	ds_read2st64_b32 v[50:51], v221 offset0:36 offset1:37
	ds_read2st64_b32 v[52:53], v221 offset0:38 offset1:39
	ds_read2st64_b32 v[62:63], v67 offset0:144 offset1:146
	ds_read2st64_b32 v[64:65], v67 offset0:148 offset1:150
	s_waitcnt lgkmcnt(0)
	v_pk_add_f32 v[22:23], v[22:23], v[50:51]
	v_pk_add_f32 v[24:25], v[24:25], v[52:53]
	v_pk_add_f32 v[22:23], v[22:23], v[78:79] op_sel_hi:[1,0]
	v_pk_add_f32 v[24:25], v[24:25], v[78:79] op_sel_hi:[1,0]
	v_pk_fma_f32 v[22:23], v[62:63], v[76:77], v[22:23] op_sel:[0,1,0] op_sel_hi:[1,1,1]
	v_pk_fma_f32 v[24:25], v[64:65], v[76:77], v[24:25] op_sel:[0,1,0] op_sel_hi:[1,1,1]
	v_pk_add_f32 v[34:35], v[34:35], v[22:23]
	v_pk_fma_f32 v[36:37], v[22:23], v[22:23], v[36:37]
	v_pk_add_f32 v[34:35], v[34:35], v[24:25]
	v_pk_fma_f32 v[36:37], v[24:25], v[24:25], v[36:37]
	s_mov_b64 s[40:41], exec
	s_and_b64 exec, exec, s[0:1]
	ds_read2st64_b32 v[50:51], v221 offset0:40 offset1:41
	ds_read2st64_b32 v[52:53], v221 offset0:42 offset1:43
	ds_read2st64_b32 v[62:63], v67 offset0:160 offset1:162
	ds_read2st64_b32 v[64:65], v67 offset0:164 offset1:166
	s_waitcnt lgkmcnt(0)
	v_pk_add_f32 v[26:27], v[26:27], v[50:51]
	v_pk_add_f32 v[28:29], v[28:29], v[52:53]
	v_pk_add_f32 v[26:27], v[26:27], v[78:79] op_sel_hi:[1,0]
	v_pk_add_f32 v[28:29], v[28:29], v[78:79] op_sel_hi:[1,0]
	v_pk_fma_f32 v[26:27], v[62:63], v[76:77], v[26:27] op_sel:[0,1,0] op_sel_hi:[1,1,1]
	v_pk_fma_f32 v[28:29], v[64:65], v[76:77], v[28:29] op_sel:[0,1,0] op_sel_hi:[1,1,1]
	v_pk_add_f32 v[34:35], v[34:35], v[26:27]
	v_pk_fma_f32 v[36:37], v[26:27], v[26:27], v[36:37]
	v_pk_add_f32 v[34:35], v[34:35], v[28:29]
	v_pk_fma_f32 v[36:37], v[28:29], v[28:29], v[36:37]
	s_mov_b64 exec, s[40:41]
	v_add_f32_e32 v34, v34, v35
	v_add_f32_e32 v36, v36, v37
	v_mov_b32_e32 v35, v34
	v_mov_b32_e32 v37, v36
	s_nop 1
	v_permlane32_swap_b32_e32 v34, v35
	v_permlane32_swap_b32_e32 v36, v37
	v_add_f32_e32 v34, v34, v35
	v_add_f32_e32 v36, v36, v37
	v_cndmask_b32_e64 v38, v36, v34, s[0:1]
	ds_write_b32 v236, v38

.LBB1_207:
	s_or_b64 exec, exec, s[40:41]
	s_andn2_b64 vcc, exec, s[30:31]
	s_mov_b64 s[2:3], -1
	s_waitcnt lgkmcnt(0)
	s_barrier
	s_cbranch_vccnz .LBB1_221
	v_mov_b32_e32 v54, v0
	s_nop 0
	v_and_b32_e32 v56, 31, v54
	v_lshlrev_b32_e32 v46, 4, v56
	v_add_u32_e32 v47, 0x25680, v46
	v_add_u32_e32 v46, 0x25880, v46
	ds_read_b128 v[50:53], v47
	ds_read_b128 v[46:49], v46
	v_ashrrev_i32_e32 v55, 5, v54
	v_lshlrev_b32_e32 v54, 3, v56
	v_mad_u32_u24 v56, v55, s64, v54
	s_waitcnt lgkmcnt(0)
	v_pk_add_f32 v[42:43], v[42:43], v[50:51] neg_lo:[0,1] neg_hi:[0,1]
	v_pk_add_f32 v[44:45], v[44:45], v[52:53] neg_lo:[0,1] neg_hi:[0,1]
	v_pk_mul_f32 v[42:43], v[46:47], v[42:43]
	v_pk_mul_f32 v[44:45], v[48:49], v[44:45]
	v_pk_add_f32 v[38:39], v[38:39], v[50:51] neg_lo:[0,1] neg_hi:[0,1]
	v_pk_add_f32 v[40:41], v[40:41], v[52:53] neg_lo:[0,1] neg_hi:[0,1]
	v_pk_mul_f32 v[38:39], v[46:47], v[38:39]
	v_pk_mul_f32 v[40:41], v[48:49], v[40:41]
	v_pk_add_f32 v[34:35], v[34:35], v[50:51] neg_lo:[0,1] neg_hi:[0,1]
	v_pk_add_f32 v[36:37], v[36:37], v[52:53] neg_lo:[0,1] neg_hi:[0,1]
	v_pk_mul_f32 v[34:35], v[46:47], v[34:35]
	v_pk_mul_f32 v[36:37], v[48:49], v[36:37]
	v_pk_add_f32 v[30:31], v[30:31], v[50:51] neg_lo:[0,1] neg_hi:[0,1]
	v_pk_add_f32 v[32:33], v[32:33], v[52:53] neg_lo:[0,1] neg_hi:[0,1]
	v_pk_mul_f32 v[30:31], v[46:47], v[30:31]
	v_pk_mul_f32 v[32:33], v[48:49], v[32:33]
	v_pk_add_f32 v[22:23], v[22:23], v[50:51] neg_lo:[0,1] neg_hi:[0,1]
	v_pk_add_f32 v[24:25], v[24:25], v[52:53] neg_lo:[0,1] neg_hi:[0,1]
	v_pk_mul_f32 v[22:23], v[46:47], v[22:23]
	v_pk_mul_f32 v[24:25], v[48:49], v[24:25]
	v_cvt_pk_f16_f32 v42, v42, v43
	v_cvt_pk_f16_f32 v43, v44, v45
	ds_write_b64 v56, v[42:43] offset:43008
	v_cvt_pk_f16_f32 v38, v38, v39
	v_cvt_pk_f16_f32 v39, v40, v41
	ds_write_b64 v56, v[38:39] offset:47360
	v_cvt_pk_f16_f32 v34, v34, v35
	v_cvt_pk_f16_f32 v35, v36, v37
	ds_write_b64 v56, v[34:35] offset:51712
	v_cvt_pk_f16_f32 v30, v30, v31
	v_cvt_pk_f16_f32 v31, v32, v33
	ds_write_b64 v56, v[30:31] offset:56064
	v_cvt_pk_f16_f32 v22, v22, v23
	v_cvt_pk_f16_f32 v23, v24, v25
	ds_write_b64 v56, v[22:23] offset:60416
	v_cmp_gt_i32_e32 vcc, 4, v55
	s_and_saveexec_b64 s[2:3], vcc
	v_pk_add_f32 v[18:19], v[18:19], v[50:51] neg_lo:[0,1] neg_hi:[0,1]
	v_pk_add_f32 v[20:21], v[20:21], v[52:53] neg_lo:[0,1] neg_hi:[0,1]
	v_pk_mul_f32 v[18:19], v[46:47], v[18:19]
	v_pk_mul_f32 v[20:21], v[48:49], v[20:21]
	v_cvt_pk_f16_f32 v18, v18, v19
	v_cvt_pk_f16_f32 v19, v20, v21
	ds_write_b64 v56, v[18:19] offset:64768
	s_or_b64 exec, exec, s[2:3]
	s_mov_b64 s[2:3], 0
	s_waitcnt lgkmcnt(0)
	s_barrier
